# grid barrier: the first workgroup of an XCD to arrive issues an unwaited buffer_wbl2 sc1 so the leader write-back later finds fewer dirty lines
# baseline (speedup 1.0000x reference)
.LBB0_190:
	s_or_b64 exec, exec, s[6:7]
	v_cvt_f32_u32_e32 v4, v2
	s_waitcnt vmcnt(0)
	v_readfirstlane_b32 s4, v3
	v_sub_u32_e32 v3, 0, v2
	v_rcp_iflag_f32_e32 v4, v4
	v_add_u32_e32 v5, s4, v1
	v_mul_f32_e32 v4, 0x4f7ffffe, v4
	v_cvt_u32_f32_e32 v4, v4
	v_mul_lo_u32 v1, v3, v4
	v_mul_hi_u32 v1, v4, v1
	v_add_u32_e32 v1, v4, v1
	v_mul_hi_u32 v1, v5, v1
	v_mul_lo_u32 v3, v1, v2
	v_sub_u32_e32 v3, v5, v3
	v_add_u32_e32 v4, 1, v1
	v_cmp_ge_u32_e32 vcc, v3, v2
	s_nop 1
	v_cndmask_b32_e32 v1, v1, v4, vcc
	v_sub_u32_e32 v4, v3, v2
	v_cndmask_b32_e32 v3, v3, v4, vcc
	v_add_u32_e32 v4, 1, v1
	v_cmp_ge_u32_e32 vcc, v3, v2
	v_add_u32_e32 v3, 1, v5
	s_nop 0
	v_cndmask_b32_e32 v1, v1, v4, vcc
	v_mul_lo_u32 v4, v2, v1
	v_add_u32_e32 v2, v4, v2
	v_cmp_ne_u32_e32 vcc, v5, v4
	s_cbranch_vccnz .Lfw_0
	buffer_wbl2 sc1
.Lfw_0:
	v_readfirstlane_b32 s99, v1
	v_cmp_ne_u32_e32 vcc, v3, v2
	s_and_saveexec_b64 s[4:5], vcc
	s_xor_b64 s[4:5], exec, s[4:5]
	s_cbranch_execz .LBB0_204
	s_waitcnt lgkmcnt(0)
	v_mov_b32_e32 v0, 0x2000
	global_load_dword v0, v0, s[2:3] offset:1024 sc1
	s_add_u32 s8, s2, 0x2400
	s_addc_u32 s9, s3, 0
	s_waitcnt vmcnt(0)
	v_cmp_eq_u32_e32 vcc, v0, v1
	s_and_saveexec_b64 s[6:7], vcc
	s_cbranch_execz .LBB0_203
	s_mov_b32 s16, 1
	s_mov_b64 s[10:11], 0
	v_mov_b32_e32 v0, 0
	s_branch .LBB0_194

.LBB0_266:
	s_or_b64 exec, exec, s[8:9]
	v_cvt_f32_u32_e32 v4, v2
	s_waitcnt vmcnt(0)
	v_readfirstlane_b32 s6, v3
	v_sub_u32_e32 v3, 0, v2
	v_rcp_iflag_f32_e32 v4, v4
	v_add_u32_e32 v5, s6, v1
	v_mul_f32_e32 v4, 0x4f7ffffe, v4
	v_cvt_u32_f32_e32 v4, v4
	v_mul_lo_u32 v1, v3, v4
	v_mul_hi_u32 v1, v4, v1
	v_add_u32_e32 v1, v4, v1
	v_mul_hi_u32 v1, v5, v1
	v_mul_lo_u32 v3, v1, v2
	v_sub_u32_e32 v3, v5, v3
	v_add_u32_e32 v4, 1, v1
	v_cmp_ge_u32_e32 vcc, v3, v2
	s_nop 1
	v_cndmask_b32_e32 v1, v1, v4, vcc
	v_sub_u32_e32 v4, v3, v2
	v_cndmask_b32_e32 v3, v3, v4, vcc
	v_add_u32_e32 v4, 1, v1
	v_cmp_ge_u32_e32 vcc, v3, v2
	v_add_u32_e32 v3, 1, v5
	s_nop 0
	v_cndmask_b32_e32 v1, v1, v4, vcc
	v_mul_lo_u32 v4, v2, v1
	v_add_u32_e32 v2, v4, v2
	v_cmp_ne_u32_e32 vcc, v5, v4
	s_cbranch_vccnz .Lfw_1
	buffer_wbl2 sc1
.Lfw_1:
	v_readfirstlane_b32 s99, v1
	v_cmp_ne_u32_e32 vcc, v3, v2
	s_and_saveexec_b64 s[6:7], vcc
	s_xor_b64 s[6:7], exec, s[6:7]
	s_cbranch_execz .LBB0_280
	s_waitcnt lgkmcnt(0)
	v_mov_b32_e32 v0, 0x2000
	global_load_dword v0, v0, s[2:3] offset:1024 sc1
	s_add_u32 s10, s2, 0x2400
	s_addc_u32 s11, s3, 0
	s_waitcnt vmcnt(0)
	v_cmp_eq_u32_e32 vcc, v0, v1
	s_and_saveexec_b64 s[8:9], vcc
	s_cbranch_execz .LBB0_279
	s_mov_b32 s16, 1
	s_mov_b64 s[12:13], 0
	v_mov_b32_e32 v0, 0
	s_branch .LBB0_270

.Lfw_3:
	v_readfirstlane_b32 s99, v1
	v_cmp_ne_u32_e32 vcc, v3, v2
	s_and_saveexec_b64 s[4:5], vcc
	s_xor_b64 s[4:5], exec, s[4:5]
	s_cbranch_execz .LBB0_704
	s_waitcnt lgkmcnt(0)
	v_mov_b32_e32 v0, 0x2000
	global_load_dword v0, v0, s[2:3] offset:1024 sc1
	s_add_u32 s10, s2, 0x2400
	s_addc_u32 s11, s3, 0
	s_waitcnt vmcnt(0)
	v_cmp_eq_u32_e32 vcc, v0, v1
	s_and_saveexec_b64 s[6:7], vcc
	s_cbranch_execz .LBB0_703
	s_mov_b32 s18, 1
	s_mov_b64 s[12:13], 0
	v_mov_b32_e32 v0, 0
	s_branch .LBB0_694

.Lfw_4:
	v_readfirstlane_b32 s99, v1
	v_cmp_ne_u32_e32 vcc, v3, v2
	s_and_saveexec_b64 s[4:5], vcc
	s_xor_b64 s[4:5], exec, s[4:5]
	s_cbranch_execz .LBB0_774
	s_waitcnt lgkmcnt(0)
	v_mov_b32_e32 v0, 0x2000
	global_load_dword v0, v0, s[2:3] offset:1024 sc1
	s_add_u32 s12, s2, 0x2400
	s_addc_u32 s13, s3, 0
	s_waitcnt vmcnt(0)
	v_cmp_eq_u32_e32 vcc, v0, v1
	s_and_saveexec_b64 s[6:7], vcc
	s_cbranch_execz .LBB0_773
	s_mov_b32 s18, 1
	s_mov_b64 s[14:15], 0
	v_mov_b32_e32 v0, 0
	s_branch .LBB0_764

.LBB0_858:
	s_or_b64 exec, exec, s[12:13]
	v_cvt_f32_u32_e32 v4, v2
	s_waitcnt vmcnt(0)
	v_readfirstlane_b32 s4, v3
	v_sub_u32_e32 v3, 0, v2
	v_rcp_iflag_f32_e32 v4, v4
	v_add_u32_e32 v5, s4, v1
	v_mul_f32_e32 v4, 0x4f7ffffe, v4
	v_cvt_u32_f32_e32 v4, v4
	v_mul_lo_u32 v1, v3, v4
	v_mul_hi_u32 v1, v4, v1
	v_add_u32_e32 v1, v4, v1
	v_mul_hi_u32 v1, v5, v1
	v_mul_lo_u32 v3, v1, v2
	v_sub_u32_e32 v3, v5, v3
	v_add_u32_e32 v4, 1, v1
	v_cmp_ge_u32_e32 vcc, v3, v2
	s_nop 1
	v_cndmask_b32_e32 v1, v1, v4, vcc
	v_sub_u32_e32 v4, v3, v2
	v_cndmask_b32_e32 v3, v3, v4, vcc
	v_add_u32_e32 v4, 1, v1
	v_cmp_ge_u32_e32 vcc, v3, v2
	v_add_u32_e32 v3, 1, v5
	s_nop 0
	v_cndmask_b32_e32 v1, v1, v4, vcc
	v_mul_lo_u32 v4, v2, v1
	v_add_u32_e32 v2, v4, v2
	v_cmp_ne_u32_e32 vcc, v5, v4
	s_cbranch_vccnz .Lfw_5
	buffer_wbl2 sc1
.Lfw_5:
	v_readfirstlane_b32 s99, v1
	v_cmp_ne_u32_e32 vcc, v3, v2
	s_and_saveexec_b64 s[4:5], vcc
	s_xor_b64 s[4:5], exec, s[4:5]
	s_cbranch_execz .LBB0_872
	s_waitcnt lgkmcnt(0)
	v_mov_b32_e32 v0, 0x2000
	global_load_dword v0, v0, s[2:3] offset:1024 sc1
	s_add_u32 s14, s2, 0x2400
	s_addc_u32 s15, s3, 0
	s_waitcnt vmcnt(0)
	v_cmp_eq_u32_e32 vcc, v0, v1
	s_and_saveexec_b64 s[12:13], vcc
	s_cbranch_execz .LBB0_871
	s_mov_b32 s18, 1
	s_mov_b64 s[16:17], 0
	v_mov_b32_e32 v0, 0
	s_branch .LBB0_862

.LBB0_948:
	s_or_b64 exec, exec, s[12:13]
	v_cvt_f32_u32_e32 v4, v2
	s_waitcnt vmcnt(0)
	v_readfirstlane_b32 s6, v3
	v_sub_u32_e32 v3, 0, v2
	v_rcp_iflag_f32_e32 v4, v4
	v_add_u32_e32 v5, s6, v1
	v_mul_f32_e32 v4, 0x4f7ffffe, v4
	v_cvt_u32_f32_e32 v4, v4
	v_mul_lo_u32 v1, v3, v4
	v_mul_hi_u32 v1, v4, v1
	v_add_u32_e32 v1, v4, v1
	v_mul_hi_u32 v1, v5, v1
	v_mul_lo_u32 v3, v1, v2
	v_sub_u32_e32 v3, v5, v3
	v_add_u32_e32 v4, 1, v1
	v_cmp_ge_u32_e32 vcc, v3, v2
	s_nop 1
	v_cndmask_b32_e32 v1, v1, v4, vcc
	v_sub_u32_e32 v4, v3, v2
	v_cndmask_b32_e32 v3, v3, v4, vcc
	v_add_u32_e32 v4, 1, v1
	v_cmp_ge_u32_e32 vcc, v3, v2
	v_add_u32_e32 v3, 1, v5
	s_nop 0
	v_cndmask_b32_e32 v1, v1, v4, vcc
	v_mul_lo_u32 v4, v2, v1
	v_add_u32_e32 v2, v4, v2
	v_cmp_ne_u32_e32 vcc, v5, v4
	s_cbranch_vccnz .Lfw_6
	buffer_wbl2 sc1
.Lfw_6:
	v_readfirstlane_b32 s99, v1
	v_cmp_ne_u32_e32 vcc, v3, v2
	s_and_saveexec_b64 s[6:7], vcc
	s_xor_b64 s[6:7], exec, s[6:7]
	s_cbranch_execz .LBB0_962
	s_waitcnt lgkmcnt(0)
	v_mov_b32_e32 v0, 0x2000
	global_load_dword v0, v0, s[4:5] offset:1024 sc1
	s_add_u32 s14, s4, 0x2400
	s_addc_u32 s15, s5, 0
	s_waitcnt vmcnt(0)
	v_cmp_eq_u32_e32 vcc, v0, v1
	s_and_saveexec_b64 s[12:13], vcc
	s_cbranch_execz .LBB0_961
	s_mov_b32 s18, 1
	s_mov_b64 s[16:17], 0
	v_mov_b32_e32 v0, 0
	s_branch .LBB0_952

.Lfw_8:
	v_readfirstlane_b32 s99, v1
	v_cmp_ne_u32_e32 vcc, v3, v2
	s_and_saveexec_b64 s[4:5], vcc
	s_xor_b64 s[4:5], exec, s[4:5]
	s_cbranch_execz .LBB0_1142
	s_waitcnt lgkmcnt(0)
	v_mov_b32_e32 v0, 0x2000
	global_load_dword v0, v0, s[2:3] offset:1024 sc1
	s_add_u32 s8, s2, 0x2400
	s_addc_u32 s9, s3, 0
	s_waitcnt vmcnt(0)
	v_cmp_eq_u32_e32 vcc, v0, v1
	s_and_saveexec_b64 s[6:7], vcc
	s_cbranch_execz .LBB0_1141
	s_mov_b32 s18, 1
	s_mov_b64 s[10:11], 0
	v_mov_b32_e32 v0, 0
	s_branch .LBB0_1132

.LBB0_1735:
	s_or_b64 exec, exec, s[8:9]
	v_cvt_f32_u32_e32 v4, v2
	s_waitcnt vmcnt(0)
	v_readfirstlane_b32 s4, v3
	v_sub_u32_e32 v3, 0, v2
	v_rcp_iflag_f32_e32 v4, v4
	v_add_u32_e32 v5, s4, v1
	v_mul_f32_e32 v4, 0x4f7ffffe, v4
	v_cvt_u32_f32_e32 v4, v4
	v_mul_lo_u32 v1, v3, v4
	v_mul_hi_u32 v1, v4, v1
	v_add_u32_e32 v1, v4, v1
	v_mul_hi_u32 v1, v5, v1
	v_mul_lo_u32 v3, v1, v2
	v_sub_u32_e32 v3, v5, v3
	v_add_u32_e32 v4, 1, v1
	v_cmp_ge_u32_e32 vcc, v3, v2
	s_nop 1
	v_cndmask_b32_e32 v1, v1, v4, vcc
	v_sub_u32_e32 v4, v3, v2
	v_cndmask_b32_e32 v3, v3, v4, vcc
	v_add_u32_e32 v4, 1, v1
	v_cmp_ge_u32_e32 vcc, v3, v2
	v_add_u32_e32 v3, 1, v5
	s_nop 0
	v_cndmask_b32_e32 v1, v1, v4, vcc
	v_mul_lo_u32 v4, v2, v1
	v_add_u32_e32 v2, v4, v2
	v_cmp_ne_u32_e32 vcc, v5, v4
	s_cbranch_vccnz .Lfw_13
	buffer_wbl2 sc1
.Lfw_13:
	v_readfirstlane_b32 s99, v1
	v_cmp_ne_u32_e32 vcc, v3, v2
	s_and_saveexec_b64 s[4:5], vcc
	s_xor_b64 s[4:5], exec, s[4:5]
	s_cbranch_execz .LBB0_1749
	s_waitcnt lgkmcnt(0)
	v_mov_b32_e32 v0, 0x2000
	global_load_dword v0, v0, s[2:3] offset:1024 sc1
	s_add_u32 s10, s2, 0x2400
	s_addc_u32 s11, s3, 0
	s_waitcnt vmcnt(0)
	v_cmp_eq_u32_e32 vcc, v0, v1
	s_and_saveexec_b64 s[8:9], vcc
	s_cbranch_execz .LBB0_1748
	s_mov_b32 s18, 1
	s_mov_b64 s[12:13], 0
	v_mov_b32_e32 v0, 0
	s_branch .LBB0_1739

.Lfw_14:
	v_readfirstlane_b32 s99, v1
	v_cmp_ne_u32_e32 vcc, v3, v2
	s_and_saveexec_b64 s[6:7], vcc
	s_xor_b64 s[6:7], exec, s[6:7]
	s_cbranch_execz .LBB0_1839
	s_waitcnt lgkmcnt(0)
	v_mov_b32_e32 v0, 0x2000
	global_load_dword v0, v0, s[4:5] offset:1024 sc1
	s_add_u32 s10, s4, 0x2400
	s_addc_u32 s11, s5, 0
	s_waitcnt vmcnt(0)
	v_cmp_eq_u32_e32 vcc, v0, v1
	s_and_saveexec_b64 s[8:9], vcc
	s_cbranch_execz .LBB0_1838
	s_mov_b32 s18, 1
	s_mov_b64 s[12:13], 0
	v_mov_b32_e32 v0, 0
	s_branch .LBB0_1829

.Lfw_18:
	v_readfirstlane_b32 s99, v1
	v_cmp_ne_u32_e32 vcc, v3, v2
	s_and_saveexec_b64 s[4:5], vcc
	s_xor_b64 s[4:5], exec, s[4:5]
	s_cbranch_execz .LBB0_2341
	s_waitcnt lgkmcnt(0)
	v_mov_b32_e32 v0, 0x2000
	global_load_dword v0, v0, s[2:3] offset:1024 sc1
	s_add_u32 s8, s2, 0x2400
	s_addc_u32 s9, s3, 0
	s_waitcnt vmcnt(0)
	v_cmp_eq_u32_e32 vcc, v0, v1
	s_and_saveexec_b64 s[6:7], vcc
	s_cbranch_execz .LBB0_2340
	s_mov_b32 s20, 1
	s_mov_b64 s[10:11], 0
	v_mov_b32_e32 v0, 0
	s_branch .LBB0_2331

.Lfw_19:
	v_readfirstlane_b32 s99, v1
	v_cmp_ne_u32_e32 vcc, v3, v2
	s_and_saveexec_b64 s[4:5], vcc
	s_xor_b64 s[4:5], exec, s[4:5]
	s_cbranch_execz .LBB0_2460
	s_waitcnt lgkmcnt(0)
	v_mov_b32_e32 v0, 0x2000
	global_load_dword v0, v0, s[2:3] offset:1024 sc1
	s_add_u32 s8, s2, 0x2400
	s_addc_u32 s9, s3, 0
	s_waitcnt vmcnt(0)
	v_cmp_eq_u32_e32 vcc, v0, v1
	s_and_saveexec_b64 s[6:7], vcc
	s_cbranch_execz .LBB0_2459
	s_mov_b32 s24, 1
	s_mov_b64 s[10:11], 0
	v_mov_b32_e32 v0, 0
	s_branch .LBB0_2450

.Lfw_20:
	v_readfirstlane_b32 s99, v1
	v_cmp_ne_u32_e32 vcc, v3, v2
	s_and_saveexec_b64 s[4:5], vcc
	s_xor_b64 s[4:5], exec, s[4:5]
	s_cbranch_execz .LBB0_2530
	s_waitcnt lgkmcnt(0)
	v_mov_b32_e32 v0, 0x2000
	global_load_dword v0, v0, s[2:3] offset:1024 sc1
	s_add_u32 s8, s2, 0x2400
	s_addc_u32 s9, s3, 0
	s_waitcnt vmcnt(0)
	v_cmp_eq_u32_e32 vcc, v0, v1
	s_and_saveexec_b64 s[6:7], vcc
	s_cbranch_execz .LBB0_2529
	s_mov_b32 s26, 1
	s_mov_b64 s[10:11], 0
	v_mov_b32_e32 v0, 0
	s_branch .LBB0_2520

.Lfw_21:
	v_readfirstlane_b32 s99, v1
	v_cmp_ne_u32_e32 vcc, v3, v2
	s_and_saveexec_b64 s[4:5], vcc
	s_xor_b64 s[4:5], exec, s[4:5]
	s_cbranch_execz .LBB0_2628
	s_waitcnt lgkmcnt(0)
	v_mov_b32_e32 v0, 0x2000
	global_load_dword v0, v0, s[2:3] offset:1024 sc1
	s_add_u32 s10, s2, 0x2400
	s_addc_u32 s11, s3, 0
	s_waitcnt vmcnt(0)
	v_cmp_eq_u32_e32 vcc, v0, v1
	s_and_saveexec_b64 s[8:9], vcc
	s_cbranch_execz .LBB0_2627
	s_mov_b32 s28, 1
	s_mov_b64 s[12:13], 0
	v_mov_b32_e32 v0, 0
	s_branch .LBB0_2618

.Lfw_22:
	v_readfirstlane_b32 s99, v1
	v_cmp_ne_u32_e32 vcc, v3, v2
	s_and_saveexec_b64 s[6:7], vcc
	s_xor_b64 s[6:7], exec, s[6:7]
	s_cbranch_execz .LBB0_2718
	s_waitcnt lgkmcnt(0)
	v_mov_b32_e32 v0, 0x2000
	global_load_dword v0, v0, s[4:5] offset:1024 sc1
	s_add_u32 s10, s4, 0x2400
	s_addc_u32 s11, s5, 0
	s_waitcnt vmcnt(0)
	v_cmp_eq_u32_e32 vcc, v0, v1
	s_and_saveexec_b64 s[8:9], vcc
	s_cbranch_execz .LBB0_2717
	s_mov_b32 s28, 1
	s_mov_b64 s[12:13], 0
	v_mov_b32_e32 v0, 0
	s_branch .LBB0_2708

.Lfw_25:
	v_readfirstlane_b32 s99, v1
	v_cmp_ne_u32_e32 vcc, v3, v2
	s_and_saveexec_b64 s[6:7], vcc
	s_xor_b64 s[6:7], exec, s[6:7]
	s_cbranch_execz .LBB0_2976
	s_waitcnt lgkmcnt(0)
	v_mov_b32_e32 v0, 0x2000
	global_load_dword v0, v0, s[4:5] offset:1024 sc1
	s_add_u32 s10, s4, 0x2400
	s_addc_u32 s11, s5, 0
	s_waitcnt vmcnt(0)
	v_cmp_eq_u32_e32 vcc, v0, v1
	s_and_saveexec_b64 s[8:9], vcc
	s_cbranch_execz .LBB0_2975
	s_mov_b32 s22, 1
	s_mov_b64 s[12:13], 0
	v_mov_b32_e32 v0, 0
	s_branch .LBB0_2966

.Lfw_27:
	v_readfirstlane_b32 s99, v1
	v_cmp_ne_u32_e32 vcc, v3, v2
	s_and_saveexec_b64 s[4:5], vcc
	s_xor_b64 s[4:5], exec, s[4:5]
	s_cbranch_execz .LBB0_3208
	s_waitcnt lgkmcnt(0)
	v_mov_b32_e32 v0, 0x2000
	global_load_dword v0, v0, s[2:3] offset:1024 sc1
	s_add_u32 s10, s2, 0x2400
	s_addc_u32 s11, s3, 0
	s_waitcnt vmcnt(0)
	v_cmp_eq_u32_e32 vcc, v0, v1
	s_and_saveexec_b64 s[6:7], vcc
	s_cbranch_execz .LBB0_3207
	s_mov_b32 s24, 1
	s_mov_b64 s[12:13], 0
	v_mov_b32_e32 v0, 0
	s_branch .LBB0_3198

.Lfw_29:
	v_readfirstlane_b32 s99, v1
	v_cmp_ne_u32_e32 vcc, v3, v2
	s_and_saveexec_b64 s[4:5], vcc
	s_xor_b64 s[4:5], exec, s[4:5]
	s_cbranch_execz .LBB0_3376
	s_waitcnt lgkmcnt(0)
	v_mov_b32_e32 v0, 0x2000
	global_load_dword v0, v0, s[2:3] offset:1024 sc1
	s_add_u32 s10, s2, 0x2400
	s_addc_u32 s11, s3, 0
	s_waitcnt vmcnt(0)
	v_cmp_eq_u32_e32 vcc, v0, v1
	s_and_saveexec_b64 s[8:9], vcc
	s_cbranch_execz .LBB0_3375
	s_mov_b32 s26, 1
	s_mov_b64 s[12:13], 0
	v_mov_b32_e32 v0, 0
	s_branch .LBB0_3366

.Lfw_30:
	v_readfirstlane_b32 s99, v1
	v_cmp_ne_u32_e32 vcc, v3, v2
	s_and_saveexec_b64 s[6:7], vcc
	s_xor_b64 s[6:7], exec, s[6:7]
	s_cbranch_execz .LBB0_3466
	s_waitcnt lgkmcnt(0)
	v_mov_b32_e32 v0, 0x2000
	global_load_dword v0, v0, s[4:5] offset:1024 sc1
	s_add_u32 s10, s4, 0x2400
	s_addc_u32 s11, s5, 0
	s_waitcnt vmcnt(0)
	v_cmp_eq_u32_e32 vcc, v0, v1
	s_and_saveexec_b64 s[8:9], vcc
	s_cbranch_execz .LBB0_3465
	s_mov_b32 s26, 1
	s_mov_b64 s[12:13], 0
	v_mov_b32_e32 v0, 0
	s_branch .LBB0_3456
